# nt hint also on the layer-0 output-projection epilogue's residual input reads
# baseline (speedup 1.0000x reference)
.LBB0_839:
	s_mul_hi_i32 s28, s76, 0x78787879
	s_lshr_b32 s30, s28, 31
	s_ashr_i32 s28, s28, 3
	s_add_i32 s50, s28, s30
	s_mul_i32 s28, s50, 0xffffffef
	s_add_i32 s28, s28, s76
	s_cmp_eq_u32 s28, 0
	s_cselect_b64 s[78:79], -1, 0
	s_and_b64 s[30:31], s[78:79], exec
	s_cselect_b32 s30, 16, s50
	s_mul_hi_i32 s31, s30, 0x6000
	s_mulk_i32 s30, 0x6000
	s_add_u32 s45, s60, s30
	s_addc_u32 s51, s69, s31
	s_lshl_b32 s30, s36, 8
	s_ashr_i32 s31, s30, 31
	v_mov_b32_e32 v132, v182
	s_lshl_b64 s[36:37], s[30:31], 2
	s_add_u32 s31, s45, s36
	v_readfirstlane_b32 s29, v132
	s_addc_u32 s37, s51, s37
	s_lshr_b32 s36, s29, 1
	s_and_b32 s45, s36, 0x60
	s_lshl_b32 s36, s45, 2
	v_lshrrev_b32_e32 v112, 1, v132
	s_add_u32 s36, s31, s36
	v_and_b32_e32 v133, 24, v112
	s_addc_u32 s37, s37, 0
	v_lshlrev_b32_e32 v112, 2, v133
	s_ashr_i32 s29, s29, 2
	v_lshl_add_u64 v[130:131], s[36:37], 0, v[112:113]
	s_mov_b64 s[36:37], 0x12000
	s_andn2_b32 s29, s29, 63
	s_ashr_i32 s77, s76, 31
	v_lshl_add_u64 v[150:151], v[130:131], 0, s[36:37]
	v_and_or_b32 v152, v132, 15, s29
	v_or_b32_e32 v112, s30, v133
	s_lshl_b64 s[30:31], s[76:77], 19
	v_readlane_b32 s36, v252, 10
	v_or_b32_e32 v160, s45, v112
	v_readlane_b32 s37, v252, 11
	s_add_u32 s76, s36, s30
	v_or_b32_e32 v158, 16, v152
	v_or_b32_e32 v156, 32, v152
	v_or_b32_e32 v154, 48, v152
	s_addc_u32 s77, s37, s31
	s_and_b64 vcc, exec, s[48:49]
	v_ashrrev_i32_e32 v161, 31, v160
	v_ashrrev_i32_e32 v153, 31, v152
	v_ashrrev_i32_e32 v159, 31, v158
	v_ashrrev_i32_e32 v157, 31, v156
	v_ashrrev_i32_e32 v155, 31, v154
	s_mov_b32 s21, s20
	s_mov_b32 s71, s66
	s_cbranch_vccz .LBB0_841
	s_ashr_i32 s51, s50, 31
	s_add_i32 s30, s28, -1
	s_lshl_b64 s[28:29], s[50:51], 24
	s_add_u32 s31, s42, s28
	s_addc_u32 s36, s43, s29
	s_and_b64 s[28:29], s[78:79], exec
	s_cselect_b32 s28, s50, s30
	v_readlane_b32 s50, v252, 14
	v_readlane_b32 s51, v252, 15
	s_cselect_b32 s30, s51, s36
	s_cselect_b32 s31, s50, s31
	s_ashr_i32 s29, s28, 31
	s_lshl_b64 s[28:29], s[28:29], 20
	s_add_u32 s78, s31, s28
	v_lshlrev_b64 v[130:131], 10, v[152:153]
	s_addc_u32 s79, s30, s29
	v_lshl_add_u64 v[176:177], v[130:131], 0, v[160:161]
	v_lshl_add_u64 v[162:163], v[176:177], 2, s[78:79]
	global_load_dwordx4 v[168:171], v[162:163], off nt
	global_load_dwordx4 v[134:137], v[150:151], off
	global_load_dwordx4 v[130:133], v[150:151], off offset:16
	global_load_dwordx4 v[172:175], v[162:163], off offset:16 nt
	v_lshlrev_b64 v[164:165], 10, v[158:159]
	v_lshl_add_u64 v[186:187], v[164:165], 0, v[160:161]
	v_lshl_add_u64 v[166:167], v[176:177], 1, s[76:77]
	v_lshl_add_u64 v[164:165], v[186:187], 2, s[78:79]
	s_mov_b64 s[28:29], 0x20000
	s_mov_b64 s[50:51], 0
	s_waitcnt vmcnt(0)
	v_pk_fma_f32 v[170:171], v[128:129], v[136:137], v[170:171]
	v_pk_fma_f32 v[168:169], v[126:127], v[134:135], v[168:169]
	v_pk_fma_f32 v[174:175], v[124:125], v[132:133], v[174:175]
	v_pk_fma_f32 v[172:173], v[122:123], v[130:131], v[172:173]
	v_cvt_pk_bf16_f32 v168, v168, v169
	v_cvt_pk_bf16_f32 v169, v170, v171
	v_cvt_pk_bf16_f32 v170, v172, v173
	v_cvt_pk_bf16_f32 v171, v174, v175
	global_store_dwordx4 v[166:167], v[168:171], off
	global_load_dwordx4 v[172:175], v[164:165], off nt
	global_load_dwordx4 v[178:181], v[164:165], off offset:16 nt
	v_lshlrev_b64 v[168:169], 10, v[156:157]
	v_lshl_add_u64 v[190:191], v[168:169], 0, v[160:161]
	v_lshl_add_u64 v[170:171], v[186:187], 1, s[76:77]
	v_lshl_add_u64 v[168:169], v[190:191], 2, s[78:79]
	s_waitcnt vmcnt(1)
	v_pk_fma_f32 v[174:175], v[120:121], v[136:137], v[174:175]
	v_pk_fma_f32 v[172:173], v[118:119], v[134:135], v[172:173]
	s_waitcnt vmcnt(0)
	v_pk_fma_f32 v[180:181], v[116:117], v[132:133], v[180:181]
	v_pk_fma_f32 v[178:179], v[114:115], v[130:131], v[178:179]
	v_cvt_pk_bf16_f32 v172, v172, v173
	v_cvt_pk_bf16_f32 v173, v174, v175
	v_cvt_pk_bf16_f32 v174, v178, v179
	v_cvt_pk_bf16_f32 v175, v180, v181
	global_store_dwordx4 v[170:171], v[172:175], off
	global_load_dwordx4 v[178:181], v[168:169], off nt
	global_load_dwordx4 v[186:189], v[168:169], off offset:16 nt
	v_lshlrev_b64 v[172:173], 10, v[154:155]
	v_lshl_add_u64 v[194:195], v[172:173], 0, v[160:161]
	v_lshl_add_u64 v[174:175], v[190:191], 1, s[76:77]
	v_lshl_add_u64 v[172:173], v[194:195], 2, s[78:79]
	s_waitcnt vmcnt(1)
	v_pk_fma_f32 v[180:181], v[110:111], v[136:137], v[180:181]
	v_pk_fma_f32 v[178:179], v[108:109], v[134:135], v[178:179]
	s_waitcnt vmcnt(0)
	v_pk_fma_f32 v[188:189], v[106:107], v[132:133], v[188:189]
	v_pk_fma_f32 v[186:187], v[104:105], v[130:131], v[186:187]
	v_cvt_pk_bf16_f32 v178, v178, v179
	v_cvt_pk_bf16_f32 v179, v180, v181
	v_cvt_pk_bf16_f32 v180, v186, v187
	v_cvt_pk_bf16_f32 v181, v188, v189
	global_store_dwordx4 v[174:175], v[178:181], off
	global_load_dwordx4 v[186:189], v[172:173], off nt
	global_load_dwordx4 v[190:193], v[172:173], off offset:16 nt
	v_lshl_add_u64 v[178:179], v[194:195], 1, s[76:77]
	v_lshl_add_u64 v[194:195], v[176:177], 0, s[28:29]
	v_lshl_add_u64 v[180:181], v[194:195], 2, s[78:79]
	s_mov_b64 s[28:29], 0x24000
	v_lshl_add_u64 v[206:207], v[176:177], 0, s[28:29]
	v_lshl_add_u64 v[194:195], v[194:195], 1, s[76:77]
	v_lshl_add_u64 v[208:209], v[206:207], 2, s[78:79]
	s_mov_b64 s[28:29], 0x28000
	v_lshl_add_u64 v[210:211], v[176:177], 0, s[28:29]
	v_lshl_add_u64 v[206:207], v[206:207], 1, s[76:77]
	v_lshl_add_u64 v[212:213], v[210:211], 2, s[78:79]
	s_mov_b64 s[28:29], 0x2c000
	v_lshl_add_u64 v[176:177], v[176:177], 0, s[28:29]
	v_lshl_add_u64 v[210:211], v[210:211], 1, s[76:77]
	v_lshl_add_u64 v[216:217], v[176:177], 2, s[78:79]
	v_lshl_add_u64 v[176:177], v[176:177], 1, s[76:77]
	s_waitcnt vmcnt(1)
	v_pk_fma_f32 v[188:189], v[102:103], v[136:137], v[188:189]
	v_pk_fma_f32 v[186:187], v[100:101], v[134:135], v[186:187]
	s_waitcnt vmcnt(0)
	v_pk_fma_f32 v[192:193], v[98:99], v[132:133], v[192:193]
	v_pk_fma_f32 v[190:191], v[96:97], v[130:131], v[190:191]
	v_cvt_pk_bf16_f32 v186, v186, v187
	v_cvt_pk_bf16_f32 v187, v188, v189
	v_cvt_pk_bf16_f32 v188, v190, v191
	v_cvt_pk_bf16_f32 v189, v192, v193
	global_store_dwordx4 v[178:179], v[186:189], off
	global_load_dwordx4 v[186:189], v[180:181], off nt
	s_nop 0
	global_load_dwordx4 v[190:193], v[180:181], off offset:16 nt
	s_waitcnt vmcnt(1)
	v_pk_fma_f32 v[188:189], v[94:95], v[136:137], v[188:189]
	v_pk_fma_f32 v[186:187], v[92:93], v[134:135], v[186:187]
	s_waitcnt vmcnt(0)
	v_pk_fma_f32 v[192:193], v[90:91], v[132:133], v[192:193]
	v_pk_fma_f32 v[190:191], v[88:89], v[130:131], v[190:191]
	v_cvt_pk_bf16_f32 v186, v186, v187
	v_cvt_pk_bf16_f32 v187, v188, v189
	v_cvt_pk_bf16_f32 v188, v190, v191
	v_cvt_pk_bf16_f32 v189, v192, v193
	global_store_dwordx4 v[194:195], v[186:189], off
	global_load_dwordx4 v[186:189], v[208:209], off nt
	s_nop 0
	global_load_dwordx4 v[190:193], v[208:209], off offset:16 nt
	s_waitcnt vmcnt(1)
	v_pk_fma_f32 v[188:189], v[86:87], v[136:137], v[188:189]
	v_pk_fma_f32 v[186:187], v[84:85], v[134:135], v[186:187]
	s_waitcnt vmcnt(0)
	v_pk_fma_f32 v[192:193], v[82:83], v[132:133], v[192:193]
	v_pk_fma_f32 v[190:191], v[80:81], v[130:131], v[190:191]
	v_cvt_pk_bf16_f32 v186, v186, v187
	v_cvt_pk_bf16_f32 v187, v188, v189
	v_cvt_pk_bf16_f32 v188, v190, v191
	v_cvt_pk_bf16_f32 v189, v192, v193
	global_store_dwordx4 v[206:207], v[186:189], off
	global_load_dwordx4 v[186:189], v[212:213], off nt
	s_nop 0
	global_load_dwordx4 v[190:193], v[212:213], off offset:16 nt
	s_waitcnt vmcnt(1)
	v_pk_fma_f32 v[188:189], v[78:79], v[136:137], v[188:189]
	v_pk_fma_f32 v[186:187], v[76:77], v[134:135], v[186:187]
	s_waitcnt vmcnt(0)
	v_pk_fma_f32 v[192:193], v[74:75], v[132:133], v[192:193]
	v_pk_fma_f32 v[190:191], v[72:73], v[130:131], v[190:191]
	v_cvt_pk_bf16_f32 v186, v186, v187
	v_cvt_pk_bf16_f32 v187, v188, v189
	v_cvt_pk_bf16_f32 v188, v190, v191
	v_cvt_pk_bf16_f32 v189, v192, v193
	global_store_dwordx4 v[210:211], v[186:189], off
	global_load_dwordx4 v[186:189], v[216:217], off nt
	s_nop 0
	global_load_dwordx4 v[190:193], v[216:217], off offset:16 nt
	s_waitcnt vmcnt(1)
	v_pk_fma_f32 v[136:137], v[70:71], v[136:137], v[188:189]
	v_pk_fma_f32 v[134:135], v[68:69], v[134:135], v[186:187]
	s_waitcnt vmcnt(0)
	v_pk_fma_f32 v[186:187], v[66:67], v[132:133], v[192:193]
	v_pk_fma_f32 v[132:133], v[64:65], v[130:131], v[190:191]
	v_cvt_pk_bf16_f32 v130, v134, v135
	v_cvt_pk_bf16_f32 v131, v136, v137
	v_cvt_pk_bf16_f32 v132, v132, v133
	v_cvt_pk_bf16_f32 v133, v186, v187
	global_store_dwordx4 v[176:177], v[130:133], off
	global_load_dwordx4 v[130:133], v[162:163], off offset:512 nt
	s_nop 0
	global_load_dwordx4 v[134:137], v[150:151], off offset:512
	global_load_dwordx4 v[186:189], v[150:151], off offset:528
	global_load_dwordx4 v[190:193], v[162:163], off offset:528 nt
	s_waitcnt vmcnt(2)
	v_pk_fma_f32 v[132:133], v[62:63], v[136:137], v[132:133]
	v_pk_fma_f32 v[130:131], v[60:61], v[134:135], v[130:131]
	s_waitcnt vmcnt(0)
	v_pk_fma_f32 v[162:163], v[58:59], v[188:189], v[192:193]
	v_pk_fma_f32 v[190:191], v[56:57], v[186:187], v[190:191]
	v_cvt_pk_bf16_f32 v130, v130, v131
	v_cvt_pk_bf16_f32 v131, v132, v133
	v_cvt_pk_bf16_f32 v132, v190, v191
	v_cvt_pk_bf16_f32 v133, v162, v163
	global_store_dwordx4 v[166:167], v[130:133], off offset:256
	global_load_dwordx4 v[130:133], v[164:165], off offset:512 nt
	s_nop 0
	global_load_dwordx4 v[162:165], v[164:165], off offset:528 nt
	s_waitcnt vmcnt(1)
	v_pk_fma_f32 v[132:133], v[54:55], v[136:137], v[132:133]
	v_pk_fma_f32 v[130:131], v[52:53], v[134:135], v[130:131]
	s_waitcnt vmcnt(0)
	v_pk_fma_f32 v[164:165], v[50:51], v[188:189], v[164:165]
	v_pk_fma_f32 v[162:163], v[48:49], v[186:187], v[162:163]
	v_cvt_pk_bf16_f32 v130, v130, v131
	v_cvt_pk_bf16_f32 v131, v132, v133
	v_cvt_pk_bf16_f32 v132, v162, v163
	v_cvt_pk_bf16_f32 v133, v164, v165
	global_store_dwordx4 v[170:171], v[130:133], off offset:256
	global_load_dwordx4 v[130:133], v[168:169], off offset:512 nt
	s_nop 0
	global_load_dwordx4 v[162:165], v[168:169], off offset:528 nt
	s_waitcnt vmcnt(1)
	v_pk_fma_f32 v[132:133], v[46:47], v[136:137], v[132:133]
	v_pk_fma_f32 v[130:131], v[44:45], v[134:135], v[130:131]
	s_waitcnt vmcnt(0)
	v_pk_fma_f32 v[164:165], v[42:43], v[188:189], v[164:165]
	v_pk_fma_f32 v[162:163], v[40:41], v[186:187], v[162:163]
	v_cvt_pk_bf16_f32 v130, v130, v131
	v_cvt_pk_bf16_f32 v131, v132, v133
	v_cvt_pk_bf16_f32 v132, v162, v163
	v_cvt_pk_bf16_f32 v133, v164, v165
	global_store_dwordx4 v[174:175], v[130:133], off offset:256
	global_load_dwordx4 v[130:133], v[172:173], off offset:512 nt
	s_nop 0
	global_load_dwordx4 v[162:165], v[172:173], off offset:528 nt
	s_waitcnt vmcnt(1)
	v_pk_fma_f32 v[132:133], v[38:39], v[136:137], v[132:133]
	v_pk_fma_f32 v[130:131], v[36:37], v[134:135], v[130:131]
	s_waitcnt vmcnt(0)
	v_pk_fma_f32 v[164:165], v[34:35], v[188:189], v[164:165]
	v_pk_fma_f32 v[162:163], v[32:33], v[186:187], v[162:163]
	v_cvt_pk_bf16_f32 v130, v130, v131
	v_cvt_pk_bf16_f32 v131, v132, v133
	v_cvt_pk_bf16_f32 v132, v162, v163
	v_cvt_pk_bf16_f32 v133, v164, v165
	global_store_dwordx4 v[178:179], v[130:133], off offset:256
	global_load_dwordx4 v[130:133], v[180:181], off offset:512 nt
	s_nop 0
	global_load_dwordx4 v[162:165], v[180:181], off offset:528 nt
	s_waitcnt vmcnt(1)
	v_pk_fma_f32 v[132:133], v[30:31], v[136:137], v[132:133]
	v_pk_fma_f32 v[130:131], v[28:29], v[134:135], v[130:131]
	s_waitcnt vmcnt(0)
	v_pk_fma_f32 v[164:165], v[26:27], v[188:189], v[164:165]
	v_pk_fma_f32 v[162:163], v[24:25], v[186:187], v[162:163]
	v_cvt_pk_bf16_f32 v130, v130, v131
	v_cvt_pk_bf16_f32 v131, v132, v133
	v_cvt_pk_bf16_f32 v132, v162, v163
	v_cvt_pk_bf16_f32 v133, v164, v165
	global_store_dwordx4 v[194:195], v[130:133], off offset:256
	global_load_dwordx4 v[130:133], v[208:209], off offset:512 nt
	s_nop 0
	global_load_dwordx4 v[162:165], v[208:209], off offset:528 nt
	s_waitcnt vmcnt(1)
	v_pk_fma_f32 v[132:133], v[22:23], v[136:137], v[132:133]
	v_pk_fma_f32 v[130:131], v[20:21], v[134:135], v[130:131]
	s_waitcnt vmcnt(0)
	v_pk_fma_f32 v[164:165], v[18:19], v[188:189], v[164:165]
	v_pk_fma_f32 v[162:163], v[16:17], v[186:187], v[162:163]
	v_cvt_pk_bf16_f32 v130, v130, v131
	v_cvt_pk_bf16_f32 v131, v132, v133
	v_cvt_pk_bf16_f32 v132, v162, v163
	v_cvt_pk_bf16_f32 v133, v164, v165
	global_store_dwordx4 v[206:207], v[130:133], off offset:256
	global_load_dwordx4 v[130:133], v[212:213], off offset:512 nt
	s_nop 0
	global_load_dwordx4 v[162:165], v[212:213], off offset:528 nt
	s_waitcnt vmcnt(1)
	v_pk_fma_f32 v[132:133], v[14:15], v[136:137], v[132:133]
	v_pk_fma_f32 v[130:131], v[12:13], v[134:135], v[130:131]
	s_waitcnt vmcnt(0)
	v_pk_fma_f32 v[164:165], v[10:11], v[188:189], v[164:165]
	v_pk_fma_f32 v[162:163], v[8:9], v[186:187], v[162:163]
	v_cvt_pk_bf16_f32 v130, v130, v131
	v_cvt_pk_bf16_f32 v131, v132, v133
	v_cvt_pk_bf16_f32 v132, v162, v163
	v_cvt_pk_bf16_f32 v133, v164, v165
	global_store_dwordx4 v[210:211], v[130:133], off offset:256
	global_load_dwordx4 v[130:133], v[216:217], off offset:512 nt
	s_nop 0
	global_load_dwordx4 v[162:165], v[216:217], off offset:528 nt
	s_waitcnt vmcnt(1)
	v_pk_fma_f32 v[132:133], v[6:7], v[136:137], v[132:133]
	v_pk_fma_f32 v[130:131], v[4:5], v[134:135], v[130:131]
	s_waitcnt vmcnt(0)
	v_pk_fma_f32 v[134:135], v[2:3], v[188:189], v[164:165]
	v_pk_fma_f32 v[136:137], v[0:1], v[186:187], v[162:163]
	v_cvt_pk_bf16_f32 v130, v130, v131
	v_cvt_pk_bf16_f32 v131, v132, v133
	v_cvt_pk_bf16_f32 v132, v136, v137
	v_cvt_pk_bf16_f32 v133, v134, v135
	global_store_dwordx4 v[176:177], v[130:133], off offset:256
	s_branch .LBB0_842
